# v13
# speedup vs baseline: 1.0789x; 1.0289x over previous
_Z14k_scatter_nodePKiS0_PjPiPKfS4_PfS5_PDF16_:
	s_mov_b32 s31, s2
	s_mov_b64 s[34:35], s[0:1]
	s_cmpk_gt_i32 s2, 0xff
	s_mov_b64 s[4:5], -1
	s_cbranch_scc0 .LBB1_4
	s_load_dwordx8 s[12:19], s[34:35], 0x20
	s_load_dwordx2 s[20:21], s[34:35], 0x40
	v_lshrrev_b32_e32 v1, 6, v0
	v_and_b32_e32 v3, 15, v0
	v_bfe_u32 v4, v0, 4, 2
	s_lshl_b32 s3, s31, 8
	s_add_i32 s3, s3, 0xffff0000
	v_lshl_add_u32 v5, v1, 5, s3
	v_add_u32_e32 v6, v5, v3
	v_readfirstlane_b32 s22, v5
	v_add_u32_e32 v7, 16, v6
	s_mov_b32 s23, 0xc350
	s_cmp_ge_i32 s22, s23
	s_cbranch_scc1 .Lk2n_end
	v_min_i32_e32 v8, 0xc34f, v6
	v_min_i32_e32 v9, 0xc34f, v7
	v_lshlrev_b32_e32 v10, 4, v4
	v_lshl_add_u32 v8, v8, 8, v10
	v_lshl_add_u32 v9, v9, 8, v10
	v_lshlrev_b32_e32 v11, 2, v3
	v_lshl_add_u32 v11, v4, 8, v11
	s_waitcnt lgkmcnt(0)
	global_load_dwordx4 v[32:35], v8, s[12:13]
	global_load_dwordx4 v[36:39], v8, s[12:13] offset:64
	global_load_dwordx4 v[40:43], v8, s[12:13] offset:128
	global_load_dwordx4 v[44:47], v8, s[12:13] offset:192
	global_load_dwordx4 v[48:51], v9, s[12:13]
	global_load_dwordx4 v[52:55], v9, s[12:13] offset:64
	global_load_dwordx4 v[56:59], v9, s[12:13] offset:128
	global_load_dwordx4 v[60:63], v9, s[12:13] offset:192
	global_load_dword v16, v11, s[14:15]
	global_load_dword v17, v11, s[14:15] offset:64
	global_load_dword v18, v11, s[14:15] offset:128
	global_load_dword v19, v11, s[14:15] offset:192
	global_load_dword v20, v11, s[14:15] offset:1024
	global_load_dword v21, v11, s[14:15] offset:1088
	global_load_dword v22, v11, s[14:15] offset:1152
	global_load_dword v23, v11, s[14:15] offset:1216
	global_load_dword v24, v11, s[14:15] offset:2048
	global_load_dword v25, v11, s[14:15] offset:2112
	global_load_dword v26, v11, s[14:15] offset:2176
	global_load_dword v27, v11, s[14:15] offset:2240
	global_load_dword v28, v11, s[14:15] offset:3072
	global_load_dword v29, v11, s[14:15] offset:3136
	global_load_dword v30, v11, s[14:15] offset:3200
	global_load_dword v31, v11, s[14:15] offset:3264
	v_cmp_gt_i32_e64 s[24:25], s23, v6
	v_cmp_gt_i32_e64 s[26:27], s23, v7
	v_cmp_gt_u32_e32 vcc, 2, v4
	v_mov_b32_e32 v12, s18
	v_mov_b32_e32 v13, s19
	v_mov_b32_e32 v14, s16
	v_mov_b32_e32 v15, s17
	v_cndmask_b32_e32 v12, v12, v14, vcc
	v_cndmask_b32_e32 v13, v13, v15, vcc
	v_and_b32_e32 v14, 1, v4
	v_lshlrev_b32_e32 v14, 4, v14
	v_mov_b32_e32 v15, 0
	v_lshl_add_u32 v88, v6, 5, v14
	v_mov_b32_e32 v89, 0
	v_lshl_add_u32 v14, v7, 5, v14
	v_lshl_add_u64 v[88:89], v[88:89], 0, v[12:13]
	v_lshl_add_u64 v[90:91], v[14:15], 0, v[12:13]
	v_lshlrev_b32_e32 v10, 3, v4
	v_lshl_add_u32 v92, v6, 7, v10
	v_lshl_add_u32 v93, v7, 7, v10
	s_waitcnt vmcnt(0)
	v_mfma_f32_16x16x4_f32 v[64:67], v16, v32, 0
	v_mfma_f32_16x16x4_f32 v[68:71], v16, v48, 0
	v_mfma_f32_16x16x4_f32 v[64:67], v17, v33, v[64:67]
	v_mfma_f32_16x16x4_f32 v[68:71], v17, v49, v[68:71]
	v_mfma_f32_16x16x4_f32 v[64:67], v18, v34, v[64:67]
	v_mfma_f32_16x16x4_f32 v[68:71], v18, v50, v[68:71]
	v_mfma_f32_16x16x4_f32 v[64:67], v19, v35, v[64:67]
	v_mfma_f32_16x16x4_f32 v[68:71], v19, v51, v[68:71]
	v_mfma_f32_16x16x4_f32 v[64:67], v20, v36, v[64:67]
	v_mfma_f32_16x16x4_f32 v[68:71], v20, v52, v[68:71]
	v_mfma_f32_16x16x4_f32 v[64:67], v21, v37, v[64:67]
	v_mfma_f32_16x16x4_f32 v[68:71], v21, v53, v[68:71]
	v_mfma_f32_16x16x4_f32 v[64:67], v22, v38, v[64:67]
	v_mfma_f32_16x16x4_f32 v[68:71], v22, v54, v[68:71]
	v_mfma_f32_16x16x4_f32 v[64:67], v23, v39, v[64:67]
	v_mfma_f32_16x16x4_f32 v[68:71], v23, v55, v[68:71]
	v_mfma_f32_16x16x4_f32 v[64:67], v24, v40, v[64:67]
	v_mfma_f32_16x16x4_f32 v[68:71], v24, v56, v[68:71]
	v_mfma_f32_16x16x4_f32 v[64:67], v25, v41, v[64:67]
	v_mfma_f32_16x16x4_f32 v[68:71], v25, v57, v[68:71]
	v_mfma_f32_16x16x4_f32 v[64:67], v26, v42, v[64:67]
	v_mfma_f32_16x16x4_f32 v[68:71], v26, v58, v[68:71]
	v_mfma_f32_16x16x4_f32 v[64:67], v27, v43, v[64:67]
	v_mfma_f32_16x16x4_f32 v[68:71], v27, v59, v[68:71]
	v_mfma_f32_16x16x4_f32 v[64:67], v28, v44, v[64:67]
	v_mfma_f32_16x16x4_f32 v[68:71], v28, v60, v[68:71]
	v_mfma_f32_16x16x4_f32 v[64:67], v29, v45, v[64:67]
	v_mfma_f32_16x16x4_f32 v[68:71], v29, v61, v[68:71]
	v_mfma_f32_16x16x4_f32 v[64:67], v30, v46, v[64:67]
	v_mfma_f32_16x16x4_f32 v[68:71], v30, v62, v[68:71]
	v_mfma_f32_16x16x4_f32 v[64:67], v31, v47, v[64:67]
	v_mfma_f32_16x16x4_f32 v[68:71], v31, v63, v[68:71]
	v_cvt_pk_f16_f32 v72, v32, v33
	v_cvt_pk_f16_f32 v73, v34, v35
	v_cvt_pk_f16_f32 v74, v36, v37
	v_cvt_pk_f16_f32 v75, v38, v39
	v_cvt_pk_f16_f32 v76, v40, v41
	v_cvt_pk_f16_f32 v77, v42, v43
	v_cvt_pk_f16_f32 v78, v44, v45
	v_cvt_pk_f16_f32 v79, v46, v47
	v_cvt_pk_f16_f32 v80, v48, v49
	v_cvt_pk_f16_f32 v81, v50, v51
	v_cvt_pk_f16_f32 v82, v52, v53
	v_cvt_pk_f16_f32 v83, v54, v55
	v_cvt_pk_f16_f32 v84, v56, v57
	v_cvt_pk_f16_f32 v85, v58, v59
	v_cvt_pk_f16_f32 v86, v60, v61
	v_cvt_pk_f16_f32 v87, v62, v63
	s_mov_b64 exec, s[24:25]
	global_store_dwordx2 v92, v[72:73], s[20:21]
	global_store_dwordx2 v92, v[74:75], s[20:21] offset:32
	global_store_dwordx2 v92, v[76:77], s[20:21] offset:64
	global_store_dwordx2 v92, v[78:79], s[20:21] offset:96
	global_store_dwordx4 v[88:89], v[64:67], off
	s_mov_b64 exec, s[26:27]
	global_store_dwordx2 v93, v[80:81], s[20:21]
	global_store_dwordx2 v93, v[82:83], s[20:21] offset:32
	global_store_dwordx2 v93, v[84:85], s[20:21] offset:64
	global_store_dwordx2 v93, v[86:87], s[20:21] offset:96
	global_store_dwordx4 v[90:91], v[68:71], off
.Lk2n_end:
	s_endpgm
.LBB1_4:
	s_andn2_b64 vcc, exec, s[4:5]
	s_cbranch_vccnz .LBB1_81
	s_load_dwordx2 s[6:7], s[34:35], 0x0
	s_mul_i32 s3, s31, 0x7a2
	v_add_u32_e32 v2, s3, v0
	v_mov_b32_e32 v1, 0
	v_mov_b32_e32 v102, -1
	s_waitcnt lgkmcnt(0)
	s_add_u32 s8, s6, 0x1e8480
	s_addc_u32 s9, s7, 0
	s_min_i32 s3, s3, 0x7997e
	s_addk_i32 s3, 0x7a2
	v_cmp_gt_i32_e32 vcc, s3, v2
	v_ashrrev_i32_e32 v3, 31, v2
	v_mov_b32_e32 v105, -1
	v_mov_b32_e32 v106, 0
	s_and_saveexec_b64 s[4:5], vcc
	s_cbranch_execz .LBB1_7
	v_lshlrev_b64 v[4:5], 2, v[2:3]
	v_lshl_add_u64 v[6:7], s[8:9], 0, v[4:5]
	v_lshl_add_u64 v[4:5], s[6:7], 0, v[4:5]
	global_load_dword v105, v[6:7], off
	global_load_dword v106, v[4:5], off
